# edge1: two-stage gather wait, vmcnt(10) before the first consumer and vmcnt(0) before the 23rd
# speedup vs baseline: 1.0034x; 1.0034x over previous
.Lprio_e1_done:
	s_mov_b32 s93, s94
	s_add_u32 s94, s94, 0x1000
	s_cmp_lt_u32 s94, 0x61a8
	s_cselect_b32 s95, s94, s93
	s_lshl_b32 s95, s95, 9
	s_add_u32 s56, s8, s95
	s_addc_u32 s57, s9, 0
	ds_bpermute_b32 v126, v125, v51
	v_sub_f32_e32 v39, v48, v67
	v_fmamk_f32 v32, v39, 0x4297576a, v65
	v_fmamk_f32 v33, v39, 0x4297576a, v76
	v_med3_f32 v35, v32, s22, v74
	v_med3_f32 v37, v33, s22, v74
	v_mul_f32_e64 v32, v35, -v35
	v_fmamk_f32 v34, v35, 0x4019be61, v75
	v_mul_f32_e64 v33, v37, -v37
	v_fmamk_f32 v35, v35, 0xc019be61, v75
	v_exp_f32_e32 v32, v32
	v_exp_f32_e32 v33, v33
	v_exp_f32_e32 v36, v35
	v_fmamk_f32 v35, v37, 0x4019be61, v75
	v_exp_f32_e32 v34, v34
	v_exp_f32_e32 v35, v35
	v_fmamk_f32 v37, v37, 0xc019be61, v75
	v_exp_f32_e32 v37, v37
	v_pk_mul_f32 v[32:33], v[48:49], v[32:33] op_sel:[1,0]
	ds_read_b128 v[28:31], v69
	ds_read_b128 v[24:27], v69 offset:1024
	ds_read_b128 v[20:23], v69 offset:2048
	ds_read_b128 v[16:19], v69 offset:3072
	ds_read_b128 v[0:3], v70
	ds_read_b128 v[4:7], v70 offset:32
	ds_read_b128 v[8:11], v70 offset:64
	ds_read_b128 v[12:15], v70 offset:96
	v_pk_mul_f32 v[44:45], v[34:35], v[32:33]
	v_pk_mul_f32 v[34:35], v[34:35], s[16:17] op_sel_hi:[1,0]
	v_mov_b32_e32 v99, v80
	v_fmamk_f32 v38, v39, 0x4297576a, v77
	v_fmamk_f32 v39, v39, 0x4297576a, v78
	v_pk_mul_f32 v[46:47], v[34:35], v[44:45]
	v_pk_mul_f32 v[34:35], v[34:35], s[16:17] op_sel_hi:[1,0]
	v_pk_mul_f32 v[80:81], v[36:37], v[32:33]
	v_pk_mul_f32 v[36:37], v[36:37], s[16:17] op_sel_hi:[1,0]
	v_med3_f32 v41, v38, s22, v74
	v_med3_f32 v43, v39, s22, v74
	v_pk_mul_f32 v[58:59], v[34:35], v[46:47]
	v_pk_mul_f32 v[34:35], v[34:35], s[16:17] op_sel_hi:[1,0]
	v_pk_mul_f32 v[82:83], v[36:37], v[80:81]
	v_pk_mul_f32 v[36:37], v[36:37], s[16:17] op_sel_hi:[1,0]
	v_mul_f32_e64 v38, v41, -v41
	v_fmamk_f32 v40, v41, 0x4019be61, v75
	v_mul_f32_e64 v39, v43, -v43
	v_fmamk_f32 v41, v41, 0xc019be61, v75
	v_pk_mul_f32 v[34:35], v[34:35], v[58:59]
	v_pk_mul_f32 v[36:37], v[36:37], v[82:83]
	v_exp_f32_e32 v38, v38
	v_exp_f32_e32 v39, v39
	v_exp_f32_e32 v42, v41
	v_fmamk_f32 v41, v43, 0x4019be61, v75
	v_cvt_pk_f16_f32 v56, v44, v46
	v_cvt_pk_f16_f32 v54, v36, v82
	v_cvt_pk_f16_f32 v57, v58, v34
	v_cvt_pk_f16_f32 v55, v80, v32
	v_exp_f32_e32 v40, v40
	v_exp_f32_e32 v41, v41
	s_waitcnt lgkmcnt(0)
	v_mfma_f32_32x32x16_f16 v[0:15], v[28:31], v[54:57], v[0:15]
	v_mul_f32_e64 v38, v49, v38
	v_mul_f32_e64 v39, v49, v39
	v_fmamk_f32 v43, v43, 0xc019be61, v75
	v_mul_f32_e64 v84, v40, v38
	v_mul_f32_e64 v85, v41, v39
	v_pk_mul_f32 v[40:41], v[40:41], s[16:17] op_sel_hi:[1,0]
	v_cvt_pk_f16_f32 v30, v45, v47
	v_pk_mul_f32 v[86:87], v[40:41], v[84:85]
	v_pk_mul_f32 v[28:29], v[40:41], s[16:17] op_sel_hi:[1,0]
	v_cvt_pk_f16_f32 v31, v59, v35
	v_pk_mul_f32 v[40:41], v[28:29], v[86:87]
	v_pk_mul_f32 v[28:29], v[28:29], s[16:17] op_sel_hi:[1,0]
	v_exp_f32_e32 v43, v43
	v_pk_mul_f32 v[88:89], v[28:29], v[40:41]
	v_cvt_pk_f16_f32 v28, v37, v83
	v_cvt_pk_f16_f32 v29, v81, v33
	v_pk_mul_f32 v[36:37], v[42:43], v[38:39]
	v_pk_mul_f32 v[42:43], v[42:43], s[16:17] op_sel_hi:[1,0]
	v_mfma_f32_32x32x16_f16 v[0:15], v[24:27], v[28:31], v[0:15]
	v_mul_f32_e64 v32, v42, v36
	v_mul_f32_e64 v33, v43, v37
	v_mul_f32_e64 v24, v42, s16
	v_mul_f32_e64 v25, v43, s16
	v_cvt_pk_f16_f32 v26, v84, v86
	v_pk_mul_f32 v[34:35], v[24:25], v[32:33]
	v_cvt_pk_f16_f32 v27, v40, v88
	v_cvt_pk_f16_f32 v24, v34, v32
	v_cvt_pk_f16_f32 v25, v36, v38
	v_cvt_pk_f16_f32 v84, v85, v87
	v_cvt_pk_f16_f32 v82, v35, v33
	v_mfma_f32_32x32x16_f16 v[0:15], v[20:23], v[24:27], v[0:15]
	ds_read_b128 v[20:23], v69 offset:4096
	v_cvt_pk_f16_f32 v85, v41, v89
	v_cvt_pk_f16_f32 v83, v37, v39
	ds_read_b128 v[32:35], v70 offset:128
	ds_read_b128 v[36:39], v70 offset:160
	ds_read_b128 v[40:43], v70 offset:192
	ds_read_b128 v[44:47], v70 offset:224
	s_nop 0
	v_add_u32_e32 v64, s12, v64
	v_perm_b32 v127, v126, v51, s64
	s_nop 0
	v_readlane_b32 s70, v127, 0
	v_readlane_b32 s71, v127, 1
	v_readlane_b32 s72, v127, 2
	v_readlane_b32 s73, v127, 3
	v_readlane_b32 s74, v127, 4
	v_readlane_b32 s75, v127, 5
	v_readlane_b32 s76, v127, 6
	v_readlane_b32 s77, v127, 7
	v_readlane_b32 s78, v127, 8
	v_readlane_b32 s79, v127, 9
	v_readlane_b32 s80, v127, 10
	v_readlane_b32 s81, v127, 11
	v_readlane_b32 s82, v127, 12
	v_readlane_b32 s83, v127, 13
	v_readlane_b32 s84, v127, 14
	v_readlane_b32 s85, v127, 15
	s_pack_ll_b32_b16 s48, s70, 0
	v_mfma_f32_32x32x16_f16 v[0:15], v[16:19], v[82:85], v[0:15]
	ds_read_b128 v[16:19], v69 offset:5120
	s_nop 0
	s_lshl_b32 s48, s48, 8
	s_and_b32 s48, s48, 0xffff00
	s_pack_ll_b32_b16 s47, s71, 0
	s_add_u32 s48, s4, s48
	s_addc_u32 s49, s5, 0
	s_waitcnt lgkmcnt(1)
	v_mfma_f32_32x32x16_f16 v[32:47], v[20:23], v[54:57], v[32:47]
	ds_read_b128 v[20:23], v69 offset:6144
	s_lshl_b32 s47, s47, 8
	s_and_b32 s47, s47, 0xffff00
	s_pack_ll_b32_b16 s46, s72, 0
	s_pack_ll_b32_b16 s45, s73, 0
	s_pack_ll_b32_b16 s44, s74, 0
	s_pack_ll_b32_b16 s43, s75, 0
	s_waitcnt lgkmcnt(1)
	v_mfma_f32_32x32x16_f16 v[32:47], v[16:19], v[28:31], v[32:47]
	s_nop 0
	s_nop 0
	s_mov_b64 vcc, 0
	s_nop 0
	s_nop 0
	s_pack_ll_b32_b16 s3, s76, 0
	s_pack_ll_b32_b16 s2, s77, 0
	s_waitcnt lgkmcnt(0)
	v_mfma_f32_32x32x16_f16 v[32:47], v[20:23], v[24:27], v[32:47]
	s_nop 0
	s_nop 0
	s_pack_ll_b32_b16 s36, s78, 0
	s_pack_ll_b32_b16 s35, s79, 0
	s_pack_ll_b32_b16 s34, s80, 0
	s_pack_ll_b32_b16 s33, s81, 0
	s_pack_ll_b32_b16 s31, s82, 0
	s_pack_ll_b32_b16 s30, s83, 0
	s_pack_ll_b32_b16 s29, s84, 0
	s_pack_ll_b32_b16 s28, s85, 0
	s_pack_hh_b32_b16 s27, s70, 0
	s_pack_hh_b32_b16 s26, s71, 0
	s_pack_hh_b32_b16 s25, s72, 0
	s_pack_hh_b32_b16 s24, s73, 0
	s_pack_hh_b32_b16 s23, s74, 0
	s_pack_hh_b32_b16 s42, s75, 0
	s_pack_hh_b32_b16 s41, s76, 0
	s_pack_hh_b32_b16 s40, s77, 0
	s_pack_hh_b32_b16 s39, s78, 0
	s_pack_hh_b32_b16 s38, s79, 0
	s_pack_hh_b32_b16 s37, s80, 0
	s_pack_hh_b32_b16 s21, s81, 0
	s_pack_hh_b32_b16 s20, s82, 0
	s_pack_hh_b32_b16 s19, s83, 0
	s_pack_hh_b32_b16 s18, s84, 0
	s_pack_hh_b32_b16 s10, s85, 0
	ds_read_b128 v[16:19], v69 offset:7168
	s_nop 0
	global_load_dwordx4 v[56:59], v124, s[56:57]
	global_load_dword v80, v124, s[56:57] offset:24
	global_load_dword v51, v124, s[56:57] offset:-8
	global_load_dword v112, v79, s[48:49]
	s_add_u32 s48, s4, s47
	s_addc_u32 s49, s5, 0
	s_lshl_b32 s46, s46, 8
	s_and_b32 s46, s46, 0xffff00
	s_add_u32 s46, s4, s46
	s_addc_u32 s47, s5, 0
	s_lshl_b32 s45, s45, 8
	s_and_b32 s45, s45, 0xffff00
	global_load_dword v110, v79, s[48:49]
	global_load_dword v108, v79, s[46:47]
	s_add_u32 s46, s4, s45
	s_addc_u32 s47, s5, 0
	s_lshl_b32 s44, s44, 8
	s_and_b32 s44, s44, 0xffff00
	s_add_u32 s44, s4, s44
	s_addc_u32 s45, s5, 0
	s_lshl_b32 s43, s43, 8
	s_and_b32 s43, s43, 0xffff00
	global_load_dword v106, v79, s[46:47]
	global_load_dword v104, v79, s[44:45]
	s_add_u32 s44, s4, s43
	s_addc_u32 s45, s5, 0
	s_lshl_b32 s3, s3, 8
	s_and_b32 s3, s3, 0xffff00
	global_load_dword v102, v79, s[44:45]
	s_add_u32 s44, s4, s3
	s_addc_u32 s45, s5, 0
	s_lshl_b32 s2, s2, 8
	s_and_b32 s2, s2, 0xffff00
	s_add_u32 s2, s4, s2
	global_load_dword v100, v79, s[44:45]
	s_addc_u32 s3, s5, 0
	global_load_dword v114, v79, s[2:3]
	s_lshl_b32 s2, s36, 8
	s_and_b32 s2, s2, 0xffff00
	s_add_u32 s2, s4, s2
	s_addc_u32 s3, s5, 0
	global_load_dword v113, v79, s[2:3]
	s_lshl_b32 s2, s35, 8
	s_and_b32 s2, s2, 0xffff00
	s_add_u32 s2, s4, s2
	s_addc_u32 s3, s5, 0
	global_load_dword v111, v79, s[2:3]
	s_lshl_b32 s2, s34, 8
	s_and_b32 s2, s2, 0xffff00
	s_add_u32 s2, s4, s2
	s_addc_u32 s3, s5, 0
	global_load_dword v109, v79, s[2:3]
	s_lshl_b32 s2, s33, 8
	s_and_b32 s2, s2, 0xffff00
	s_add_u32 s2, s4, s2
	s_addc_u32 s3, s5, 0
	global_load_dword v107, v79, s[2:3]
	s_lshl_b32 s2, s31, 8
	s_and_b32 s2, s2, 0xffff00
	s_add_u32 s2, s4, s2
	s_addc_u32 s3, s5, 0
	global_load_dword v105, v79, s[2:3]
	s_lshl_b32 s2, s30, 8
	s_and_b32 s2, s2, 0xffff00
	s_add_u32 s2, s4, s2
	s_addc_u32 s3, s5, 0
	global_load_dword v103, v79, s[2:3]
	s_lshl_b32 s2, s29, 8
	s_and_b32 s2, s2, 0xffff00
	s_add_u32 s2, s4, s2
	s_addc_u32 s3, s5, 0
	global_load_dword v101, v79, s[2:3]
	s_lshl_b32 s2, s28, 8
	s_and_b32 s2, s2, 0xffff00
	s_add_u32 s2, s4, s2
	s_addc_u32 s3, s5, 0
	global_load_dword v98, v79, s[2:3]
	s_lshl_b32 s2, s27, 8
	s_and_b32 s2, s2, 0xffff00
	s_add_u32 s2, s4, s2
	s_addc_u32 s3, s5, 0
	global_load_dword v97, v79, s[2:3]
	s_lshl_b32 s2, s26, 8
	s_and_b32 s2, s2, 0xffff00
	s_add_u32 s2, s4, s2
	s_addc_u32 s3, s5, 0
	global_load_dword v96, v79, s[2:3]
	s_lshl_b32 s2, s25, 8
	s_and_b32 s2, s2, 0xffff00
	s_add_u32 s2, s4, s2
	s_addc_u32 s3, s5, 0
	global_load_dword v94, v79, s[2:3]
	s_lshl_b32 s2, s24, 8
	s_and_b32 s2, s2, 0xffff00
	s_add_u32 s2, s4, s2
	s_addc_u32 s3, s5, 0
	global_load_dword v91, v79, s[2:3]
	s_lshl_b32 s2, s23, 8
	s_and_b32 s2, s2, 0xffff00
	s_add_u32 s2, s4, s2
	s_addc_u32 s3, s5, 0
	global_load_dword v93, v79, s[2:3]
	s_lshl_b32 s2, s42, 8
	s_and_b32 s2, s2, 0xffff00
	s_add_u32 s2, s4, s2
	s_addc_u32 s3, s5, 0
	global_load_dword v90, v79, s[2:3]
	s_lshl_b32 s2, s41, 8
	s_and_b32 s2, s2, 0xffff00
	s_add_u32 s2, s4, s2
	s_addc_u32 s3, s5, 0
	global_load_dword v88, v79, s[2:3]
	s_lshl_b32 s2, s40, 8
	s_and_b32 s2, s2, 0xffff00
	s_add_u32 s2, s4, s2
	s_addc_u32 s3, s5, 0
	global_load_dword v86, v79, s[2:3]
	s_lshl_b32 s2, s39, 8
	s_and_b32 s2, s2, 0xffff00
	s_nop 0
	s_nop 0
	s_add_u32 s2, s4, s2
	s_waitcnt lgkmcnt(0)
	v_mfma_f32_32x32x16_f16 v[32:47], v[16:19], v[82:85], v[32:47]
	v_exp_f32_e32 v0, v0
	v_exp_f32_e32 v1, v1
	s_addc_u32 s3, s5, 0
	global_load_dword v85, v79, s[2:3]
	s_lshl_b32 s2, s38, 8
	s_and_b32 s2, s2, 0xffff00
	s_nop 0
	s_nop 0
	s_add_u32 s2, s4, s2
	v_exp_f32_e32 v6, v6
	v_exp_f32_e32 v7, v7
	s_addc_u32 s3, s5, 0
	global_load_dword v83, v79, s[2:3]
	s_lshl_b32 s2, s37, 8
	s_and_b32 s2, s2, 0xffff00
	s_add_u32 s2, s4, s2
	s_addc_u32 s3, s5, 0
	global_load_dword v92, v79, s[2:3]
	s_lshl_b32 s2, s21, 8
	s_and_b32 s2, s2, 0xffff00
	s_add_u32 s2, s4, s2
	s_addc_u32 s3, s5, 0
	global_load_dword v89, v79, s[2:3]
	s_lshl_b32 s2, s20, 8
	s_and_b32 s2, s2, 0xffff00
	s_add_u32 s2, s4, s2
	s_addc_u32 s3, s5, 0
	s_lshl_b32 s19, s19, 8
	s_and_b32 s19, s19, 0xffff00
	s_add_u32 s20, s4, s19
	s_addc_u32 s21, s5, 0
	s_lshl_b32 s18, s18, 8
	s_and_b32 s18, s18, 0xffff00
	s_add_u32 s18, s4, s18
	s_addc_u32 s19, s5, 0
	s_lshl_b32 s10, s10, 8
	s_and_b32 s10, s10, 0xffff00
	s_add_u32 s24, s4, s10
	s_addc_u32 s25, s5, 0
	global_load_dword v87, v79, s[2:3]
	global_load_dword v84, v79, s[20:21]
	global_load_dword v82, v79, s[18:19]
	global_load_dword v81, v79, s[24:25]
	v_pk_add_f32 v[0:1], v[0:1], 1.0 op_sel_hi:[1,0]
	s_nop 0
	s_nop 0
	v_exp_f32_e32 v16, v4
	v_exp_f32_e32 v17, v5
	v_log_f32_e32 v4, v0
	v_log_f32_e32 v5, v1
	s_nop 0
	s_nop 0
	v_exp_f32_e32 v2, v2
	v_exp_f32_e32 v3, v3
	v_pk_add_f32 v[6:7], v[6:7], 1.0 op_sel_hi:[1,0]
	v_log_f32_e32 v6, v6
	v_log_f32_e32 v7, v7
	v_pk_add_f32 v[0:1], v[16:17], 1.0 op_sel_hi:[1,0]
	v_pk_add_f32 v[2:3], v[2:3], 1.0 op_sel_hi:[1,0]
	v_log_f32_e32 v0, v0
	v_log_f32_e32 v1, v1
	v_exp_f32_e32 v18, v8
	v_exp_f32_e32 v19, v9
	v_log_f32_e32 v8, v2
	v_log_f32_e32 v9, v3
	v_pk_mul_f32 v[2:3], v[48:49], v[6:7] op_sel:[1,0]
	s_nop 0
	s_nop 0
	v_pk_mul_f32 v[0:1], v[48:49], v[0:1] op_sel:[1,0]
	s_nop 0
	s_nop 0
	v_cvt_pk_f16_f32 v3, v2, v3
	v_cvt_pk_f16_f32 v2, v0, v1
	v_pk_mul_f32 v[0:1], v[48:49], v[8:9] op_sel:[1,0]
	v_pk_mul_f32 v[4:5], v[48:49], v[4:5] op_sel:[1,0]
	s_nop 0
	s_nop 0
	s_nop 0
	s_nop 0
	v_cvt_pk_f16_f32 v1, v0, v1
	v_cvt_pk_f16_f32 v0, v4, v5
	v_pk_add_f32 v[4:5], v[18:19], 1.0 op_sel_hi:[1,0]
	v_exp_f32_e32 v6, v10
	v_exp_f32_e32 v7, v11
	v_exp_f32_e32 v8, v12
	v_exp_f32_e32 v9, v13
	v_exp_f32_e32 v10, v14
	v_exp_f32_e32 v11, v15
	v_pk_add_f32 v[8:9], v[8:9], 1.0 op_sel_hi:[1,0]
	v_pk_add_f32 v[10:11], v[10:11], 1.0 op_sel_hi:[1,0]
	v_pk_add_f32 v[6:7], v[6:7], 1.0 op_sel_hi:[1,0]
	v_log_f32_e32 v8, v8
	v_log_f32_e32 v9, v9
	v_log_f32_e32 v10, v10
	v_log_f32_e32 v11, v11
	ds_read_b128 v[12:15], v71
	v_log_f32_e32 v6, v6
	v_log_f32_e32 v7, v7
	v_log_f32_e32 v4, v4
	v_log_f32_e32 v5, v5
	v_pk_mul_f32 v[8:9], v[48:49], v[8:9] op_sel:[1,0]
	v_pk_mul_f32 v[10:11], v[48:49], v[10:11] op_sel:[1,0]
	v_cvt_pk_f16_f32 v118, v8, v9
	v_cvt_pk_f16_f32 v119, v10, v11
	v_pk_mul_f32 v[10:11], v[48:49], v[6:7] op_sel:[1,0]
	ds_read_b128 v[6:9], v71 offset:1024
	s_waitcnt lgkmcnt(1)
	v_mfma_f32_32x32x16_f16 v[16:31], v[0:3], v[12:15], 0
	s_nop 0
	s_nop 0
	v_mul_f32_e64 v4, v49, v4
	v_mul_f32_e64 v5, v49, v5
	v_exp_f32_e32 v32, v32
	v_exp_f32_e32 v33, v33
	s_nop 0
	s_nop 0
	v_cvt_pk_f16_f32 v117, v10, v11
	v_cvt_pk_f16_f32 v116, v4, v5
	v_exp_f32_e32 v36, v36
	v_exp_f32_e32 v37, v37
	v_pk_add_f32 v[32:33], v[32:33], 1.0 op_sel_hi:[1,0]
	s_waitcnt lgkmcnt(0)
	v_mfma_f32_32x32x16_f16 v[16:31], v[116:119], v[6:9], v[16:31]
	v_log_f32_e32 v54, v32
	v_log_f32_e32 v55, v33
	v_pk_add_f32 v[32:33], v[36:37], 1.0 op_sel_hi:[1,0]
	s_nop 0
	s_nop 0
	ds_read_b128 v[4:7], v71 offset:4096
	ds_read_b128 v[120:123], v71 offset:5120
	v_exp_f32_e32 v36, v38
	v_exp_f32_e32 v37, v39
	s_nop 0
	s_nop 0
	s_waitcnt lgkmcnt(1)
	v_mfma_f32_32x32x16_f16 v[0:15], v[0:3], v[4:7], 0
	v_exp_f32_e32 v34, v34
	v_exp_f32_e32 v35, v35
	v_pk_add_f32 v[36:37], v[36:37], 1.0 op_sel_hi:[1,0]
	v_log_f32_e32 v32, v32
	v_log_f32_e32 v33, v33
	v_log_f32_e32 v36, v36
	v_log_f32_e32 v37, v37
	v_pk_add_f32 v[34:35], v[34:35], 1.0 op_sel_hi:[1,0]
	v_pk_mul_f32 v[32:33], v[48:49], v[32:33] op_sel:[1,0]
	v_log_f32_e32 v38, v34
	v_log_f32_e32 v39, v35
	v_pk_mul_f32 v[34:35], v[48:49], v[36:37] op_sel:[1,0]
	v_pk_mul_f32 v[36:37], v[48:49], v[54:55] op_sel:[1,0]
	v_cvt_pk_f16_f32 v35, v34, v35
	v_cvt_pk_f16_f32 v34, v32, v33
	v_pk_mul_f32 v[32:33], v[48:49], v[38:39] op_sel:[1,0]
	s_waitcnt lgkmcnt(0)
	v_mfma_f32_32x32x16_f16 v[0:15], v[116:119], v[120:123], v[0:15]
	v_cvt_pk_f16_f32 v33, v32, v33
	v_cvt_pk_f16_f32 v32, v36, v37
	ds_read_b128 v[36:39], v71 offset:2048
	ds_read_b128 v[116:119], v71 offset:3072
	s_nop 0
	s_nop 0
	v_exp_f32_e32 v55, v44
	v_exp_f32_e32 v115, v45
	s_waitcnt lgkmcnt(1)
	v_mfma_f32_32x32x16_f16 v[16:31], v[32:35], v[36:39], v[16:31]
	ds_read_b128 v[36:39], v71 offset:6144
	v_exp_f32_e32 v44, v40
	v_exp_f32_e32 v45, v41
	v_exp_f32_e32 v52, v42
	v_exp_f32_e32 v54, v43
	ds_read_b128 v[40:43], v71 offset:7168
	s_nop 0
	s_waitcnt lgkmcnt(1)
	v_mfma_f32_32x32x16_f16 v[0:15], v[32:35], v[36:39], v[0:15]
	v_add_f32_e64 v34, v44, 1.0
	v_add_f32_e64 v35, v45, 1.0
	s_nop 0
	s_nop 0
	s_nop 0
	v_log_f32_e32 v36, v34
	v_log_f32_e32 v37, v35
	v_exp_f32_e32 v34, v46
	v_exp_f32_e32 v35, v47
	s_nop 0
	s_nop 0
	v_add_f32_e64 v32, v55, 1.0
	v_add_f32_e64 v33, v115, 1.0
	v_pk_add_f32 v[34:35], v[34:35], 1.0 op_sel_hi:[1,0]
	v_log_f32_e32 v32, v32
	v_log_f32_e32 v33, v33
	v_log_f32_e32 v34, v34
	v_log_f32_e32 v35, v35
	v_add_f32_e64 v38, v52, 1.0
	v_add_f32_e64 v39, v54, 1.0
	v_pk_mul_f32 v[32:33], v[48:49], v[32:33] op_sel:[1,0]
	v_log_f32_e32 v38, v38
	v_log_f32_e32 v39, v39
	v_pk_mul_f32 v[34:35], v[48:49], v[34:35] op_sel:[1,0]
	v_pk_mul_f32 v[36:37], v[48:49], v[36:37] op_sel:[1,0]
	v_cvt_pk_f16_f32 v35, v34, v35
	v_cvt_pk_f16_f32 v34, v32, v33
	v_pk_mul_f32 v[32:33], v[48:49], v[38:39] op_sel:[1,0]
	v_mov_b32_e32 v54, v53
	v_cvt_pk_f16_f32 v33, v32, v33
	v_cvt_pk_f16_f32 v32, v36, v37
	v_cvt_f16_f32_e32 v36, v49
	v_mov_b32_e32 v55, v53
	v_mfma_f32_32x32x16_f16 v[16:31], v[32:35], v[116:119], v[16:31]
	v_cmp_ne_u32_sdwa s[20:21], v95, v50 src0_sel:DWORD src1_sel:WORD_1
	v_cmp_ne_u32_sdwa s[18:19], v99, v50 src0_sel:WORD_1 src1_sel:WORD_1
	s_bitcmp1_b32 s20, 0
	v_cmp_lt_i32_e64 s[2:3], s13, v64
	s_cselect_b64 s[20:21], -1, 0
	s_bitcmp0_b32 s18, 0
	s_waitcnt lgkmcnt(0)
	v_mfma_f32_32x32x16_f16 v[0:15], v[32:35], v[40:43], v[0:15]
	v_cndmask_b32_e64 v32, 0, v36, s[0:1]
	v_pack_b32_f16 v52, v32, 0
	ds_read_b128 v[32:35], v72
	ds_read_b128 v[36:39], v72 offset:1024
	s_waitcnt vmcnt(10)
	s_nop 0
	s_waitcnt lgkmcnt(1)
	v_mfma_f32_32x32x16_f16 v[16:31], v[52:55], v[32:35], v[16:31]
	v_mov_b64_e32 v[32:33], 0
	s_nop 0
	s_waitcnt lgkmcnt(0)
	v_mfma_f32_32x32x16_f16 v[0:15], v[52:55], v[36:39], v[0:15]
	s_nop 11
	v_permlane32_swap_b32_e32 v16, v0
	v_permlane32_swap_b32_e32 v17, v1
	v_permlane32_swap_b32_e32 v18, v2
	v_permlane32_swap_b32_e32 v19, v3
	v_permlane32_swap_b32_e32 v20, v4
	v_permlane32_swap_b32_e32 v21, v5
	v_permlane32_swap_b32_e32 v22, v6
	v_permlane32_swap_b32_e32 v23, v7
	v_permlane32_swap_b32_e32 v24, v8
	v_permlane32_swap_b32_e32 v25, v9
	v_permlane32_swap_b32_e32 v26, v10
	v_permlane32_swap_b32_e32 v27, v11
	v_permlane32_swap_b32_e32 v28, v12
	v_permlane32_swap_b32_e32 v29, v13
	v_permlane32_swap_b32_e32 v30, v14
	v_permlane32_swap_b32_e32 v31, v15
	v_fma_mix_f32 v32, v16, v112, v32 op_sel:[0,1,0] op_sel_hi:[0,1,0]
	v_fma_mix_f32 v33, v16, v112, v33 op_sel_hi:[0,1,0]
	s_cbranch_scc1 .LBB4_13
	v_readlane_b32 s10, v50, 0
	s_bfe_u32 s19, s10, 0x80008
	v_lshl_or_b32 v16, s19, 7, v73
	ds_read_u16 v16, v16
	s_bfe_u32 s10, s10, 0x100010
	s_lshl_b32 s10, s10, 8
	s_add_u32 s58, s60, s10
	s_addc_u32 s59, s61, 0
	s_cmp_lg_u64 s[20:21], 0
	s_cselect_b32 s58, s58, s62
	s_cselect_b32 s59, s59, s63
	s_nop 0
	s_waitcnt lgkmcnt(0)
	v_fma_mix_f32 v16, v16, v33, v32 op_sel_hi:[1,0,0]
	s_nop 0
	s_mov_b64 s[20:21], -1
	v_mov_b64_e32 v[32:33], 0
	s_nop 0
	global_store_dword v79, v16, s[58:59] sc1

.LBB4_55:
	s_bitcmp0_b32 s18, 22
	s_waitcnt vmcnt(0)
	v_fma_mix_f32 v32, v10, v88, v32 op_sel:[0,1,0] op_sel_hi:[0,1,0]
	v_fma_mix_f32 v33, v10, v88, v33 op_sel_hi:[0,1,0]
	s_cbranch_scc1 .LBB4_57
	v_readlane_b32 s10, v50, 22
	s_bfe_u32 s19, s10, 0x80008
	v_lshl_or_b32 v0, s19, 7, v73
	ds_read_u16 v2, v0
	s_bfe_u32 s10, s10, 0x100010
	s_lshl_b32 s10, s10, 8
	s_add_u32 s58, s60, s10
	s_addc_u32 s59, s61, 0
	s_cmp_lg_u64 s[20:21], 0
	s_cselect_b32 s58, s58, s62
	s_cselect_b32 s59, s59, s63
	s_nop 0
	s_waitcnt lgkmcnt(0)
	v_fma_mix_f32 v2, v2, v33, v32 op_sel_hi:[1,0,0]
	s_nop 0
	s_mov_b64 s[20:21], -1
	v_mov_b64_e32 v[32:33], 0
	s_nop 0
	global_store_dword v79, v2, s[58:59] sc1
